# post2 phase: a token row's loads requested one row ahead (after the previous row's last chunk); first-row waits counted separately (on top of v19)
# speedup vs baseline: 1.0066x; 1.0066x over previous
.LBB0_1670:
	s_or_b64 exec, exec, s[10:11]
	v_ashrrev_i32_e32 v2, 6, v4
	v_add_u32_e32 v2, s84, v2
	s_movk_i32 s3, 0x2000
	v_cmp_gt_i32_e32 vcc, s3, v2
	s_waitcnt lgkmcnt(0)
	s_barrier
	s_and_saveexec_b64 s[10:11], vcc
	s_cbranch_execz .LBB0_1675
	v_and_b32_e32 v3, 63, v4
	v_mov_b32_e32 v13, 0
	v_lshlrev_b32_e32 v12, 4, v3
	v_lshlrev_b32_e32 v10, 3, v3
	v_mov_b32_e32 v11, v13
	v_lshl_add_u64 v[4:5], s[8:9], 0, v[12:13]
	v_lshl_add_u64 v[6:7], s[16:17], 0, v[10:11]
	s_mov_b64 s[8:9], 0x40c00000
	s_add_u32 s12, s12, 0x54c00000
	v_lshl_add_u64 v[6:7], v[6:7], 0, s[8:9]
	v_lshl_add_u64 v[8:9], s[20:21], 0, v[10:11]
	s_mov_b64 s[8:9], 0x34400000
	s_addc_u32 s13, s13, 0
	v_lshl_add_u64 v[8:9], v[8:9], 0, s[8:9]
	v_lshl_add_u64 v[10:11], s[22:23], 0, v[10:11]
	s_mov_b64 s[8:9], 0x1a300000
	v_lshlrev_b32_e32 v14, 2, v3
	v_mov_b32_e32 v15, v13
	s_add_u32 s14, s14, 0x54c10000
	v_lshl_add_u64 v[10:11], v[10:11], 0, s[8:9]
	v_add_u32_e32 v86, 0, v12
	v_lshl_add_u64 v[12:13], s[18:19], 0, v[14:15]
	s_mov_b64 s[8:9], 0x50c00000
	s_addc_u32 s15, s15, 0
	v_lshl_add_u64 v[12:13], v[12:13], 0, s[8:9]
	v_cmp_eq_u32_e64 s[8:9], 0, v3
	s_lshl_b32 s20, s46, 3
	s_mov_b64 s[16:17], 0
	s_mov_b32 s21, 0xffff0000
	s_movk_i32 s22, 0x7fff
	s_movk_i32 s23, 0x1000
	s_movk_i32 s24, 0x3000
	v_mov_b32_e32 v87, 0x358637bd
	s_mov_b32 s25, 0x800000
	s_mov_b32 s26, 0xda24260
	s_mov_b32 s27, 0x40c0c00
	s_movk_i32 s28, 0x1fff
	v_mov_b32_e32 v88, 1
	s_mov_b64 s[98:99], 0x1000
	s_mov_b32 s100, 1
	v_mov_b32_e32 v254, v2
	v_ashrrev_i32_e32 v255, 31, v254
	v_lshlrev_b64 v[250:251], 13, v[254:255]
	v_lshlrev_b64 v[252:253], 14, v[254:255]
	v_lshl_add_u64 v[250:251], v[6:7], 0, v[250:251]
	v_lshl_add_u64 v[252:253], v[4:5], 0, v[252:253]
	v_lshl_add_u64 v[242:243], v[250:251], 0, s[98:99]
	v_lshl_add_u64 v[244:245], v[252:253], 0, s[98:99]
	v_lshl_add_u64 v[246:247], v[244:245], 0, s[98:99]
	v_lshl_add_u64 v[248:249], v[246:247], 0, s[98:99]
	global_load_dwordx2 v[178:179], v[250:251], off
	global_load_dwordx2 v[180:181], v[250:251], off offset:512
	global_load_dwordx2 v[182:183], v[250:251], off offset:1024
	global_load_dwordx2 v[184:185], v[250:251], off offset:1536
	global_load_dwordx2 v[186:187], v[250:251], off offset:2048
	global_load_dwordx2 v[188:189], v[250:251], off offset:2560
	global_load_dwordx2 v[190:191], v[250:251], off offset:3072
	global_load_dwordx2 v[192:193], v[250:251], off offset:3584
	global_load_dwordx2 v[194:195], v[242:243], off
	global_load_dwordx2 v[196:197], v[242:243], off offset:512
	global_load_dwordx2 v[198:199], v[242:243], off offset:1024
	global_load_dwordx2 v[200:201], v[242:243], off offset:1536
	global_load_dwordx2 v[202:203], v[242:243], off offset:2048
	global_load_dwordx2 v[204:205], v[242:243], off offset:2560
	global_load_dwordx2 v[206:207], v[242:243], off offset:3072
	global_load_dwordx2 v[208:209], v[242:243], off offset:3584
	global_load_dwordx4 v[210:213], v[252:253], off
	global_load_dwordx4 v[214:217], v[252:253], off offset:1024
	global_load_dwordx4 v[218:221], v[252:253], off offset:2048
	global_load_dwordx4 v[222:225], v[252:253], off offset:3072
	global_load_dwordx4 v[226:229], v[244:245], off
	global_load_dwordx4 v[230:233], v[244:245], off offset:1024
	global_load_dwordx4 v[234:237], v[244:245], off offset:2048
	global_load_dwordx4 v[238:241], v[244:245], off offset:3072
	s_branch .LBB0_1673

.LBB0_1673:
	v_ashrrev_i32_e32 v3, 31, v2
	v_lshlrev_b64 v[52:53], 13, v[2:3]
	v_lshl_add_u64 v[42:43], v[6:7], 0, v[52:53]
	v_lshlrev_b64 v[16:17], 14, v[2:3]
	s_waitcnt lgkmcnt(0)
	v_lshl_add_u64 v[66:67], v[4:5], 0, v[16:17]
	s_cmp_lg_u32 s100, 0
	s_cbranch_scc1 .Lp6_first0
	s_waitcnt vmcnt(42)
	s_branch .Lp6_go0
.Lp6_first0:
	s_waitcnt vmcnt(7)
.Lp6_go0:
	v_mov_b32_e32 v14, v178
	v_mov_b32_e32 v15, v179
	v_mov_b32_e32 v16, v210
	v_mov_b32_e32 v17, v211
	v_mov_b32_e32 v18, v212
	v_mov_b32_e32 v19, v213
	v_lshl_add_u64 v[46:47], v[8:9], 0, v[52:53]
	v_add_co_u32_e32 v62, vcc, s3, v66
	v_lshlrev_b32_e32 v20, 16, v14
	v_and_b32_e32 v21, 0xffff0000, v14
	v_lshlrev_b32_e32 v14, 16, v15
	v_and_b32_e32 v15, 0xffff0000, v15
	v_pk_add_f32 v[14:15], v[18:19], v[14:15]
	v_pk_add_f32 v[16:17], v[16:17], v[20:21]
	v_and_b32_sdwa v20, v15, v88 dst_sel:DWORD dst_unused:UNUSED_PAD src0_sel:WORD_1 src1_sel:DWORD
	v_and_b32_sdwa v19, v16, v88 dst_sel:DWORD dst_unused:UNUSED_PAD src0_sel:WORD_1 src1_sel:DWORD
	v_and_b32_sdwa v21, v17, v88 dst_sel:DWORD dst_unused:UNUSED_PAD src0_sel:WORD_1 src1_sel:DWORD
	v_and_b32_sdwa v18, v14, v88 dst_sel:DWORD dst_unused:UNUSED_PAD src0_sel:WORD_1 src1_sel:DWORD
	v_add3_u32 v22, v16, v19, s22
	v_add3_u32 v19, v15, v20, s22
	v_add3_u32 v20, v17, v21, s22
	v_add3_u32 v18, v14, v18, s22
	v_and_b32_e32 v19, 0xffff0000, v19
	v_and_b32_e32 v20, 0xffff0000, v20
	v_or_b32_sdwa v19, v19, v18 dst_sel:DWORD dst_unused:UNUSED_PAD src0_sel:DWORD src1_sel:WORD_1
	v_or_b32_sdwa v18, v20, v22 dst_sel:DWORD dst_unused:UNUSED_PAD src0_sel:DWORD src1_sel:WORD_1
	global_store_dwordx2 v[46:47], v[18:19], off
	global_load_dwordx4 v[210:213], v[246:247], off
	s_nop 0
	s_cmp_lg_u32 s100, 0
	s_cbranch_scc1 .Lp6_first1
	s_waitcnt vmcnt(43)
	s_branch .Lp6_go1

.Lp6_go1:
	v_mov_b32_e32 v18, v180
	v_mov_b32_e32 v19, v181
	v_mov_b32_e32 v20, v214
	v_mov_b32_e32 v21, v215
	v_mov_b32_e32 v22, v216
	v_mov_b32_e32 v23, v217
	v_addc_co_u32_e32 v63, vcc, 0, v67, vcc
	v_add_co_u32_e32 v44, vcc, s23, v66
	v_lshlrev_b32_e32 v24, 16, v18
	v_and_b32_e32 v25, 0xffff0000, v18
	v_lshlrev_b32_e32 v18, 16, v19
	v_and_b32_e32 v19, 0xffff0000, v19
	v_pk_add_f32 v[18:19], v[22:23], v[18:19]
	v_pk_add_f32 v[20:21], v[20:21], v[24:25]
	v_and_b32_sdwa v24, v19, v88 dst_sel:DWORD dst_unused:UNUSED_PAD src0_sel:WORD_1 src1_sel:DWORD
	v_and_b32_sdwa v23, v20, v88 dst_sel:DWORD dst_unused:UNUSED_PAD src0_sel:WORD_1 src1_sel:DWORD
	v_and_b32_sdwa v25, v21, v88 dst_sel:DWORD dst_unused:UNUSED_PAD src0_sel:WORD_1 src1_sel:DWORD
	v_and_b32_sdwa v22, v18, v88 dst_sel:DWORD dst_unused:UNUSED_PAD src0_sel:WORD_1 src1_sel:DWORD
	v_add3_u32 v26, v20, v23, s22
	v_add3_u32 v23, v19, v24, s22
	v_add3_u32 v24, v21, v25, s22
	v_add3_u32 v22, v18, v22, s22
	v_and_b32_e32 v23, 0xffff0000, v23
	v_and_b32_e32 v24, 0xffff0000, v24
	v_or_b32_sdwa v23, v23, v22 dst_sel:DWORD dst_unused:UNUSED_PAD src0_sel:DWORD src1_sel:WORD_1
	v_or_b32_sdwa v22, v24, v26 dst_sel:DWORD dst_unused:UNUSED_PAD src0_sel:DWORD src1_sel:WORD_1
	global_store_dwordx2 v[46:47], v[22:23], off offset:512
	global_load_dwordx4 v[214:217], v[246:247], off offset:1024
	s_nop 0
	s_cmp_lg_u32 s100, 0
	s_cbranch_scc1 .Lp6_first2
	s_waitcnt vmcnt(44)
	s_branch .Lp6_go2
.Lp6_first2:
	s_waitcnt vmcnt(9)
.Lp6_go2:
	v_mov_b32_e32 v22, v182
	v_mov_b32_e32 v23, v183
	v_mov_b32_e32 v24, v218
	v_mov_b32_e32 v25, v219
	v_mov_b32_e32 v26, v220
	v_mov_b32_e32 v27, v221
	v_addc_co_u32_e32 v45, vcc, 0, v67, vcc
	v_add_co_u32_e32 v74, vcc, s23, v42
	v_lshlrev_b32_e32 v28, 16, v22
	v_and_b32_e32 v29, 0xffff0000, v22
	v_lshlrev_b32_e32 v22, 16, v23
	v_and_b32_e32 v23, 0xffff0000, v23
	v_pk_add_f32 v[22:23], v[26:27], v[22:23]
	v_pk_add_f32 v[24:25], v[24:25], v[28:29]
	v_and_b32_sdwa v28, v23, v88 dst_sel:DWORD dst_unused:UNUSED_PAD src0_sel:WORD_1 src1_sel:DWORD
	v_and_b32_sdwa v27, v24, v88 dst_sel:DWORD dst_unused:UNUSED_PAD src0_sel:WORD_1 src1_sel:DWORD
	v_and_b32_sdwa v29, v25, v88 dst_sel:DWORD dst_unused:UNUSED_PAD src0_sel:WORD_1 src1_sel:DWORD
	v_and_b32_sdwa v26, v22, v88 dst_sel:DWORD dst_unused:UNUSED_PAD src0_sel:WORD_1 src1_sel:DWORD
	v_add3_u32 v30, v24, v27, s22
	v_add3_u32 v27, v23, v28, s22
	v_add3_u32 v28, v25, v29, s22
	v_add3_u32 v26, v22, v26, s22
	v_and_b32_e32 v27, 0xffff0000, v27
	v_and_b32_e32 v28, 0xffff0000, v28
	v_or_b32_sdwa v27, v27, v26 dst_sel:DWORD dst_unused:UNUSED_PAD src0_sel:DWORD src1_sel:WORD_1
	v_or_b32_sdwa v26, v28, v30 dst_sel:DWORD dst_unused:UNUSED_PAD src0_sel:DWORD src1_sel:WORD_1
	global_store_dwordx2 v[46:47], v[26:27], off offset:1024
	global_load_dwordx4 v[218:221], v[246:247], off offset:2048
	s_nop 0
	s_cmp_lg_u32 s100, 0
	s_cbranch_scc1 .Lp6_first3
	s_waitcnt vmcnt(45)
	s_branch .Lp6_go3
.Lp6_first3:
	s_waitcnt vmcnt(10)
.Lp6_go3:
	v_mov_b32_e32 v26, v184
	v_mov_b32_e32 v27, v185
	v_mov_b32_e32 v28, v222
	v_mov_b32_e32 v29, v223
	v_mov_b32_e32 v30, v224
	v_mov_b32_e32 v31, v225
	v_addc_co_u32_e32 v75, vcc, 0, v43, vcc
	v_add_co_u32_e32 v56, vcc, s23, v46
	v_lshlrev_b32_e32 v32, 16, v26
	v_and_b32_e32 v33, 0xffff0000, v26
	v_lshlrev_b32_e32 v26, 16, v27
	v_and_b32_e32 v27, 0xffff0000, v27
	v_pk_add_f32 v[26:27], v[30:31], v[26:27]
	v_pk_add_f32 v[28:29], v[28:29], v[32:33]
	v_and_b32_sdwa v32, v27, v88 dst_sel:DWORD dst_unused:UNUSED_PAD src0_sel:WORD_1 src1_sel:DWORD
	v_and_b32_sdwa v31, v28, v88 dst_sel:DWORD dst_unused:UNUSED_PAD src0_sel:WORD_1 src1_sel:DWORD
	v_and_b32_sdwa v33, v29, v88 dst_sel:DWORD dst_unused:UNUSED_PAD src0_sel:WORD_1 src1_sel:DWORD
	v_and_b32_sdwa v30, v26, v88 dst_sel:DWORD dst_unused:UNUSED_PAD src0_sel:WORD_1 src1_sel:DWORD
	v_add3_u32 v34, v28, v31, s22
	v_add3_u32 v31, v27, v32, s22
	v_add3_u32 v32, v29, v33, s22
	v_add3_u32 v30, v26, v30, s22
	v_and_b32_e32 v31, 0xffff0000, v31
	v_and_b32_e32 v32, 0xffff0000, v32
	v_or_b32_sdwa v31, v31, v30 dst_sel:DWORD dst_unused:UNUSED_PAD src0_sel:DWORD src1_sel:WORD_1
	v_or_b32_sdwa v30, v32, v34 dst_sel:DWORD dst_unused:UNUSED_PAD src0_sel:DWORD src1_sel:WORD_1
	global_store_dwordx2 v[46:47], v[30:31], off offset:1536
	global_load_dwordx4 v[222:225], v[246:247], off offset:3072
	s_cmp_lg_u32 s100, 0
	s_cbranch_scc1 .Lp6_first4
	s_waitcnt vmcnt(46)
	s_branch .Lp6_go4
.Lp6_first4:
	s_waitcnt vmcnt(11)
.Lp6_go4:
	v_mov_b32_e32 v34, v186
	v_mov_b32_e32 v35, v187
	v_mov_b32_e32 v30, v226
	v_mov_b32_e32 v31, v227
	v_mov_b32_e32 v32, v228
	v_mov_b32_e32 v33, v229
	v_addc_co_u32_e32 v57, vcc, 0, v47, vcc
	v_add_co_u32_e32 v82, vcc, s24, v66
	v_lshlrev_b32_e32 v36, 16, v34
	v_and_b32_e32 v37, 0xffff0000, v34
	v_lshlrev_b32_e32 v34, 16, v35
	v_and_b32_e32 v35, 0xffff0000, v35
	v_pk_add_f32 v[30:31], v[30:31], v[36:37]
	v_pk_add_f32 v[32:33], v[32:33], v[34:35]
	v_and_b32_sdwa v35, v30, v88 dst_sel:DWORD dst_unused:UNUSED_PAD src0_sel:WORD_1 src1_sel:DWORD
	v_and_b32_sdwa v36, v33, v88 dst_sel:DWORD dst_unused:UNUSED_PAD src0_sel:WORD_1 src1_sel:DWORD
	v_and_b32_sdwa v37, v31, v88 dst_sel:DWORD dst_unused:UNUSED_PAD src0_sel:WORD_1 src1_sel:DWORD
	v_and_b32_sdwa v34, v32, v88 dst_sel:DWORD dst_unused:UNUSED_PAD src0_sel:WORD_1 src1_sel:DWORD
	v_add3_u32 v38, v30, v35, s22
	v_add3_u32 v35, v33, v36, s22
	v_add3_u32 v36, v31, v37, s22
	v_add3_u32 v34, v32, v34, s22
	v_and_b32_e32 v35, 0xffff0000, v35
	v_and_b32_e32 v36, 0xffff0000, v36
	v_or_b32_sdwa v35, v35, v34 dst_sel:DWORD dst_unused:UNUSED_PAD src0_sel:DWORD src1_sel:WORD_1
	v_or_b32_sdwa v34, v36, v38 dst_sel:DWORD dst_unused:UNUSED_PAD src0_sel:DWORD src1_sel:WORD_1
	global_store_dwordx2 v[46:47], v[34:35], off offset:2048
	global_load_dwordx4 v[226:229], v[248:249], off
	v_addc_co_u32_e32 v83, vcc, 0, v67, vcc
	s_cmp_lg_u32 s100, 0
	s_cbranch_scc1 .Lp6_first5
	s_waitcnt vmcnt(47)
	s_branch .Lp6_go5
.Lp6_first5:
	s_waitcnt vmcnt(12)
.Lp6_go5:
	v_mov_b32_e32 v38, v188
	v_mov_b32_e32 v39, v189
	v_mov_b32_e32 v34, v230
	v_mov_b32_e32 v35, v231
	v_mov_b32_e32 v36, v232
	v_mov_b32_e32 v37, v233
	v_cmp_lt_i32_e32 vcc, v157, v154
	v_lshlrev_b32_e32 v40, 16, v38
	v_and_b32_e32 v41, 0xffff0000, v38
	v_lshlrev_b32_e32 v38, 16, v39
	v_and_b32_e32 v39, 0xffff0000, v39
	v_pk_add_f32 v[34:35], v[34:35], v[40:41]
	v_pk_add_f32 v[36:37], v[36:37], v[38:39]
	v_and_b32_sdwa v39, v34, v88 dst_sel:DWORD dst_unused:UNUSED_PAD src0_sel:WORD_1 src1_sel:DWORD
	v_and_b32_sdwa v40, v37, v88 dst_sel:DWORD dst_unused:UNUSED_PAD src0_sel:WORD_1 src1_sel:DWORD
	v_and_b32_sdwa v41, v35, v88 dst_sel:DWORD dst_unused:UNUSED_PAD src0_sel:WORD_1 src1_sel:DWORD
	v_and_b32_sdwa v38, v36, v88 dst_sel:DWORD dst_unused:UNUSED_PAD src0_sel:WORD_1 src1_sel:DWORD
	v_add3_u32 v48, v34, v39, s22
	v_add3_u32 v39, v37, v40, s22
	v_add3_u32 v40, v35, v41, s22
	v_add3_u32 v38, v36, v38, s22
	v_and_b32_e32 v39, 0xffff0000, v39
	v_and_b32_e32 v40, 0xffff0000, v40
	v_or_b32_sdwa v39, v39, v38 dst_sel:DWORD dst_unused:UNUSED_PAD src0_sel:DWORD src1_sel:WORD_1
	v_or_b32_sdwa v38, v40, v48 dst_sel:DWORD dst_unused:UNUSED_PAD src0_sel:DWORD src1_sel:WORD_1
	global_store_dwordx2 v[46:47], v[38:39], off offset:2560
	global_load_dwordx4 v[230:233], v[248:249], off offset:1024
	s_nop 0
	s_cmp_lg_u32 s100, 0
	s_cbranch_scc1 .Lp6_first6
	s_waitcnt vmcnt(48)
	s_branch .Lp6_go6
.Lp6_first6:
	s_waitcnt vmcnt(13)
.Lp6_go6:
	v_mov_b32_e32 v38, v190
	v_mov_b32_e32 v39, v191
	v_mov_b32_e32 v48, v234
	v_mov_b32_e32 v49, v235
	v_mov_b32_e32 v50, v236
	v_mov_b32_e32 v51, v237
	v_lshlrev_b32_e32 v40, 16, v38
	v_and_b32_e32 v41, 0xffff0000, v38
	v_lshlrev_b32_e32 v38, 16, v39
	v_and_b32_e32 v39, 0xffff0000, v39
	v_pk_add_f32 v[38:39], v[50:51], v[38:39]
	v_pk_add_f32 v[40:41], v[48:49], v[40:41]
	v_and_b32_sdwa v50, v39, v88 dst_sel:DWORD dst_unused:UNUSED_PAD src0_sel:WORD_1 src1_sel:DWORD
	v_and_b32_sdwa v49, v40, v88 dst_sel:DWORD dst_unused:UNUSED_PAD src0_sel:WORD_1 src1_sel:DWORD
	v_and_b32_sdwa v51, v41, v88 dst_sel:DWORD dst_unused:UNUSED_PAD src0_sel:WORD_1 src1_sel:DWORD
	v_and_b32_sdwa v48, v38, v88 dst_sel:DWORD dst_unused:UNUSED_PAD src0_sel:WORD_1 src1_sel:DWORD
	v_add3_u32 v54, v40, v49, s22
	v_add3_u32 v49, v39, v50, s22
	v_add3_u32 v50, v41, v51, s22
	v_add3_u32 v48, v38, v48, s22
	v_and_b32_e32 v49, 0xffff0000, v49
	v_and_b32_e32 v50, 0xffff0000, v50
	v_or_b32_sdwa v49, v49, v48 dst_sel:DWORD dst_unused:UNUSED_PAD src0_sel:DWORD src1_sel:WORD_1
	v_or_b32_sdwa v48, v50, v54 dst_sel:DWORD dst_unused:UNUSED_PAD src0_sel:DWORD src1_sel:WORD_1
	global_store_dwordx2 v[46:47], v[48:49], off offset:3072
	global_load_dwordx4 v[234:237], v[248:249], off offset:2048
	s_nop 0
	s_cmp_lg_u32 s100, 0
	s_cbranch_scc1 .Lp6_first7
	s_waitcnt vmcnt(49)
	s_branch .Lp6_go7

.Lp6_go7:
	v_mov_b32_e32 v54, v192
	v_mov_b32_e32 v55, v193
	v_mov_b32_e32 v48, v238
	v_mov_b32_e32 v49, v239
	v_mov_b32_e32 v50, v240
	v_mov_b32_e32 v51, v241
	v_mul_f32_e32 v102, v39, v39
	v_lshlrev_b32_e32 v42, 16, v54
	v_and_b32_e32 v43, 0xffff0000, v54
	v_lshlrev_b32_e32 v44, 16, v55
	v_and_b32_e32 v45, 0xffff0000, v55
	v_pk_add_f32 v[42:43], v[48:49], v[42:43]
	v_pk_add_f32 v[44:45], v[50:51], v[44:45]
	v_and_b32_sdwa v49, v42, v88 dst_sel:DWORD dst_unused:UNUSED_PAD src0_sel:WORD_1 src1_sel:DWORD
	v_and_b32_sdwa v50, v45, v88 dst_sel:DWORD dst_unused:UNUSED_PAD src0_sel:WORD_1 src1_sel:DWORD
	v_and_b32_sdwa v51, v43, v88 dst_sel:DWORD dst_unused:UNUSED_PAD src0_sel:WORD_1 src1_sel:DWORD
	v_and_b32_sdwa v48, v44, v88 dst_sel:DWORD dst_unused:UNUSED_PAD src0_sel:WORD_1 src1_sel:DWORD
	v_add3_u32 v54, v42, v49, s22
	v_add3_u32 v49, v45, v50, s22
	v_add3_u32 v50, v43, v51, s22
	v_add3_u32 v48, v44, v48, s22
	v_and_b32_e32 v49, 0xffff0000, v49
	v_and_b32_e32 v50, 0xffff0000, v50
	v_or_b32_sdwa v49, v49, v48 dst_sel:DWORD dst_unused:UNUSED_PAD src0_sel:DWORD src1_sel:WORD_1
	v_or_b32_sdwa v48, v50, v54 dst_sel:DWORD dst_unused:UNUSED_PAD src0_sel:DWORD src1_sel:WORD_1
	global_store_dwordx2 v[46:47], v[48:49], off offset:3584
	global_load_dwordx4 v[238:241], v[248:249], off offset:3072
	s_waitcnt vmcnt(14)
	v_mov_b32_e32 v54, v194
	v_mov_b32_e32 v55, v195
	v_mov_b32_e32 v48, v210
	v_mov_b32_e32 v49, v211
	v_mov_b32_e32 v50, v212
	v_mov_b32_e32 v51, v213
	v_lshlrev_b32_e32 v58, 16, v54
	v_and_b32_e32 v59, 0xffff0000, v54
	v_lshlrev_b32_e32 v46, 16, v55
	v_and_b32_e32 v47, 0xffff0000, v55
	v_pk_add_f32 v[46:47], v[50:51], v[46:47]
	v_pk_add_f32 v[48:49], v[48:49], v[58:59]
	v_and_b32_sdwa v54, v47, v88 dst_sel:DWORD dst_unused:UNUSED_PAD src0_sel:WORD_1 src1_sel:DWORD
	v_and_b32_sdwa v51, v48, v88 dst_sel:DWORD dst_unused:UNUSED_PAD src0_sel:WORD_1 src1_sel:DWORD
	v_and_b32_sdwa v55, v49, v88 dst_sel:DWORD dst_unused:UNUSED_PAD src0_sel:WORD_1 src1_sel:DWORD
	v_and_b32_sdwa v50, v46, v88 dst_sel:DWORD dst_unused:UNUSED_PAD src0_sel:WORD_1 src1_sel:DWORD
	v_add3_u32 v58, v48, v51, s22
	v_add3_u32 v51, v47, v54, s22
	v_add3_u32 v54, v49, v55, s22
	v_add3_u32 v50, v46, v50, s22
	v_and_b32_e32 v51, 0xffff0000, v51
	v_and_b32_e32 v54, 0xffff0000, v54
	v_or_b32_sdwa v51, v51, v50 dst_sel:DWORD dst_unused:UNUSED_PAD src0_sel:DWORD src1_sel:WORD_1
	v_or_b32_sdwa v50, v54, v58 dst_sel:DWORD dst_unused:UNUSED_PAD src0_sel:DWORD src1_sel:WORD_1
	global_store_dwordx2 v[56:57], v[50:51], off
	s_nop 0
	s_waitcnt vmcnt(13)
	v_mov_b32_e32 v50, v196
	v_mov_b32_e32 v51, v197
	v_mov_b32_e32 v58, v214
	v_mov_b32_e32 v59, v215
	v_mov_b32_e32 v60, v216
	v_mov_b32_e32 v61, v217
	v_lshlrev_b32_e32 v54, 16, v50
	v_and_b32_e32 v55, 0xffff0000, v50
	v_lshlrev_b32_e32 v50, 16, v51
	v_and_b32_e32 v51, 0xffff0000, v51
	v_pk_add_f32 v[50:51], v[60:61], v[50:51]
	v_pk_add_f32 v[54:55], v[58:59], v[54:55]
	v_and_b32_sdwa v60, v51, v88 dst_sel:DWORD dst_unused:UNUSED_PAD src0_sel:WORD_1 src1_sel:DWORD
	v_and_b32_sdwa v59, v54, v88 dst_sel:DWORD dst_unused:UNUSED_PAD src0_sel:WORD_1 src1_sel:DWORD
	v_and_b32_sdwa v61, v55, v88 dst_sel:DWORD dst_unused:UNUSED_PAD src0_sel:WORD_1 src1_sel:DWORD
	v_and_b32_sdwa v58, v50, v88 dst_sel:DWORD dst_unused:UNUSED_PAD src0_sel:WORD_1 src1_sel:DWORD
	v_add3_u32 v64, v54, v59, s22
	v_add3_u32 v59, v51, v60, s22
	v_add3_u32 v60, v55, v61, s22
	v_add3_u32 v58, v50, v58, s22
	v_and_b32_e32 v59, 0xffff0000, v59
	v_and_b32_e32 v60, 0xffff0000, v60
	v_or_b32_sdwa v59, v59, v58 dst_sel:DWORD dst_unused:UNUSED_PAD src0_sel:DWORD src1_sel:WORD_1
	v_or_b32_sdwa v58, v60, v64 dst_sel:DWORD dst_unused:UNUSED_PAD src0_sel:DWORD src1_sel:WORD_1
	global_store_dwordx2 v[56:57], v[58:59], off offset:512
	s_nop 0
	s_waitcnt vmcnt(12)
	v_mov_b32_e32 v58, v198
	v_mov_b32_e32 v59, v199
	v_mov_b32_e32 v68, v218
	v_mov_b32_e32 v69, v219
	v_mov_b32_e32 v70, v220
	v_mov_b32_e32 v71, v221
	v_lshlrev_b32_e32 v60, 16, v58
	v_and_b32_e32 v61, 0xffff0000, v58
	v_lshlrev_b32_e32 v58, 16, v59
	v_and_b32_e32 v59, 0xffff0000, v59
	v_pk_add_f32 v[58:59], v[70:71], v[58:59]
	v_pk_add_f32 v[60:61], v[68:69], v[60:61]
	v_and_b32_sdwa v68, v59, v88 dst_sel:DWORD dst_unused:UNUSED_PAD src0_sel:WORD_1 src1_sel:DWORD
	v_and_b32_sdwa v65, v60, v88 dst_sel:DWORD dst_unused:UNUSED_PAD src0_sel:WORD_1 src1_sel:DWORD
	v_and_b32_sdwa v69, v61, v88 dst_sel:DWORD dst_unused:UNUSED_PAD src0_sel:WORD_1 src1_sel:DWORD
	v_and_b32_sdwa v64, v58, v88 dst_sel:DWORD dst_unused:UNUSED_PAD src0_sel:WORD_1 src1_sel:DWORD
	v_add3_u32 v70, v60, v65, s22
	v_add3_u32 v65, v59, v68, s22
	v_add3_u32 v68, v61, v69, s22
	v_add3_u32 v64, v58, v64, s22
	v_and_b32_e32 v65, 0xffff0000, v65
	v_and_b32_e32 v68, 0xffff0000, v68
	v_or_b32_sdwa v65, v65, v64 dst_sel:DWORD dst_unused:UNUSED_PAD src0_sel:DWORD src1_sel:WORD_1
	v_or_b32_sdwa v64, v68, v70 dst_sel:DWORD dst_unused:UNUSED_PAD src0_sel:DWORD src1_sel:WORD_1
	global_store_dwordx2 v[56:57], v[64:65], off offset:1024
	s_nop 0
	s_waitcnt vmcnt(11)
	v_mov_b32_e32 v64, v200
	v_mov_b32_e32 v65, v201
	v_mov_b32_e32 v68, v222
	v_mov_b32_e32 v69, v223
	v_mov_b32_e32 v70, v224
	v_mov_b32_e32 v71, v225
	v_lshlrev_b32_e32 v72, 16, v64
	v_and_b32_e32 v73, 0xffff0000, v64
	v_lshlrev_b32_e32 v62, 16, v65
	v_and_b32_e32 v63, 0xffff0000, v65
	v_pk_add_f32 v[62:63], v[70:71], v[62:63]
	v_pk_add_f32 v[64:65], v[68:69], v[72:73]
	v_and_b32_sdwa v70, v63, v88 dst_sel:DWORD dst_unused:UNUSED_PAD src0_sel:WORD_1 src1_sel:DWORD
	v_and_b32_sdwa v69, v64, v88 dst_sel:DWORD dst_unused:UNUSED_PAD src0_sel:WORD_1 src1_sel:DWORD
	v_and_b32_sdwa v71, v65, v88 dst_sel:DWORD dst_unused:UNUSED_PAD src0_sel:WORD_1 src1_sel:DWORD
	v_and_b32_sdwa v68, v62, v88 dst_sel:DWORD dst_unused:UNUSED_PAD src0_sel:WORD_1 src1_sel:DWORD
	v_add3_u32 v72, v64, v69, s22
	v_add3_u32 v69, v63, v70, s22
	v_add3_u32 v70, v65, v71, s22
	v_add3_u32 v68, v62, v68, s22
	v_and_b32_e32 v69, 0xffff0000, v69
	v_and_b32_e32 v70, 0xffff0000, v70
	v_or_b32_sdwa v69, v69, v68 dst_sel:DWORD dst_unused:UNUSED_PAD src0_sel:DWORD src1_sel:WORD_1
	v_or_b32_sdwa v68, v70, v72 dst_sel:DWORD dst_unused:UNUSED_PAD src0_sel:DWORD src1_sel:WORD_1
	global_store_dwordx2 v[56:57], v[68:69], off offset:1536
	s_waitcnt vmcnt(10)
	v_mov_b32_e32 v72, v202
	v_mov_b32_e32 v73, v203
	v_mov_b32_e32 v68, v226
	v_mov_b32_e32 v69, v227
	v_mov_b32_e32 v70, v228
	v_mov_b32_e32 v71, v229
	v_lshlrev_b32_e32 v76, 16, v72
	v_and_b32_e32 v77, 0xffff0000, v72
	v_lshlrev_b32_e32 v66, 16, v73
	v_and_b32_e32 v67, 0xffff0000, v73
	v_pk_add_f32 v[66:67], v[70:71], v[66:67]
	v_pk_add_f32 v[68:69], v[68:69], v[76:77]
	v_and_b32_sdwa v72, v67, v88 dst_sel:DWORD dst_unused:UNUSED_PAD src0_sel:WORD_1 src1_sel:DWORD
	v_and_b32_sdwa v71, v68, v88 dst_sel:DWORD dst_unused:UNUSED_PAD src0_sel:WORD_1 src1_sel:DWORD
	v_and_b32_sdwa v73, v69, v88 dst_sel:DWORD dst_unused:UNUSED_PAD src0_sel:WORD_1 src1_sel:DWORD
	v_and_b32_sdwa v70, v66, v88 dst_sel:DWORD dst_unused:UNUSED_PAD src0_sel:WORD_1 src1_sel:DWORD
	v_add3_u32 v76, v68, v71, s22
	v_add3_u32 v71, v67, v72, s22
	v_add3_u32 v72, v69, v73, s22
	v_add3_u32 v70, v66, v70, s22
	v_and_b32_e32 v71, 0xffff0000, v71
	v_and_b32_e32 v72, 0xffff0000, v72
	v_or_b32_sdwa v71, v71, v70 dst_sel:DWORD dst_unused:UNUSED_PAD src0_sel:DWORD src1_sel:WORD_1
	v_or_b32_sdwa v70, v72, v76 dst_sel:DWORD dst_unused:UNUSED_PAD src0_sel:DWORD src1_sel:WORD_1
	global_store_dwordx2 v[56:57], v[70:71], off offset:2048
	s_nop 0
	s_waitcnt vmcnt(9)
	v_mov_b32_e32 v70, v204
	v_mov_b32_e32 v71, v205
	v_mov_b32_e32 v76, v230
	v_mov_b32_e32 v77, v231
	v_mov_b32_e32 v78, v232
	v_mov_b32_e32 v79, v233
	v_lshlrev_b32_e32 v72, 16, v70
	v_and_b32_e32 v73, 0xffff0000, v70
	v_lshlrev_b32_e32 v70, 16, v71
	v_and_b32_e32 v71, 0xffff0000, v71
	v_pk_add_f32 v[70:71], v[78:79], v[70:71]
	v_pk_add_f32 v[72:73], v[76:77], v[72:73]
	v_and_b32_sdwa v78, v71, v88 dst_sel:DWORD dst_unused:UNUSED_PAD src0_sel:WORD_1 src1_sel:DWORD
	v_and_b32_sdwa v77, v72, v88 dst_sel:DWORD dst_unused:UNUSED_PAD src0_sel:WORD_1 src1_sel:DWORD
	v_and_b32_sdwa v79, v73, v88 dst_sel:DWORD dst_unused:UNUSED_PAD src0_sel:WORD_1 src1_sel:DWORD
	v_and_b32_sdwa v76, v70, v88 dst_sel:DWORD dst_unused:UNUSED_PAD src0_sel:WORD_1 src1_sel:DWORD
	v_add3_u32 v80, v72, v77, s22
	v_add3_u32 v77, v71, v78, s22
	v_add3_u32 v78, v73, v79, s22
	v_add3_u32 v76, v70, v76, s22
	v_and_b32_e32 v77, 0xffff0000, v77
	v_and_b32_e32 v78, 0xffff0000, v78
	v_or_b32_sdwa v77, v77, v76 dst_sel:DWORD dst_unused:UNUSED_PAD src0_sel:DWORD src1_sel:WORD_1
	v_or_b32_sdwa v76, v78, v80 dst_sel:DWORD dst_unused:UNUSED_PAD src0_sel:DWORD src1_sel:WORD_1
	global_store_dwordx2 v[56:57], v[76:77], off offset:2560
	s_nop 0
	s_waitcnt vmcnt(8)
	v_mov_b32_e32 v76, v206
	v_mov_b32_e32 v77, v207
	v_mov_b32_e32 v94, v234
	v_mov_b32_e32 v95, v235
	v_mov_b32_e32 v96, v236
	v_mov_b32_e32 v97, v237
	v_cndmask_b32_e32 v78, v1, v157, vcc
	v_cmp_lt_i32_e32 vcc, v158, v154
	v_lshlrev_b32_e32 v92, 2, v78
	v_lshlrev_b64 v[80:81], 12, v[2:3]
	v_cndmask_b32_e32 v79, v1, v158, vcc
	v_cmp_lt_i32_e32 vcc, v159, v154
	v_lshlrev_b32_e32 v91, 2, v79
	v_pk_mul_f32 v[78:79], v[14:15], v[14:15]
	v_cndmask_b32_e32 v84, v1, v159, vcc
	v_cmp_lt_i32_e32 vcc, v160, v154
	v_lshlrev_b32_e32 v90, 2, v84
	s_nop 0
	v_cndmask_b32_e32 v85, v1, v160, vcc
	v_lshlrev_b32_e32 v89, 2, v85
	v_pk_mul_f32 v[84:85], v[16:17], v[16:17]
	v_cmp_lt_i32_e32 vcc, v156, v154
	v_pk_mov_b32 v[98:99], v[84:85], v[78:79] op_sel:[1,0]
	v_mov_b32_e32 v85, v79
	v_pk_add_f32 v[78:79], v[98:99], v[84:85]
	v_pk_mul_f32 v[84:85], v[18:19], v[18:19]
	v_pk_mul_f32 v[98:99], v[20:21], v[20:21]
	v_pk_add_f32 v[78:79], v[78:79], v[78:79] op_sel:[0,1] op_sel_hi:[1,0]
	v_pk_mov_b32 v[100:101], v[98:99], v[84:85] op_sel:[1,0]
	v_mov_b32_e32 v99, v85
	v_pk_add_f32 v[84:85], v[100:101], v[98:99]
	v_mul_f32_e32 v79, v28, v28
	v_pk_add_f32 v[84:85], v[84:85], v[84:85] op_sel:[0,1] op_sel_hi:[1,0]
	v_mul_f32_e32 v98, v25, v25
	v_mul_f32_e32 v85, v29, v29
	v_mul_f32_e32 v100, v23, v23
	v_pk_add_f32 v[84:85], v[78:79], v[84:85]
	v_pk_fma_f32 v[98:99], v[24:25], v[24:25], v[98:99] op_sel_hi:[1,1,0]
	v_pk_fma_f32 v[100:101], v[22:23], v[22:23], v[100:101] op_sel_hi:[1,1,0]
	v_mul_f32_e32 v99, v26, v26
	v_mul_f32_e32 v101, v27, v27
	v_pk_add_f32 v[98:99], v[98:99], v[100:101]
	v_cndmask_b32_e32 v93, v1, v156, vcc
	v_pk_add_f32 v[84:85], v[84:85], v[98:99]
	v_pk_mul_f32 v[98:99], v[32:33], v[32:33]
	v_pk_add_f32 v[84:85], v[84:85], v[84:85] op_sel:[0,1] op_sel_hi:[1,0]
	v_cmp_lt_i32_e32 vcc, v155, v154
	v_mul_f32_e32 v85, v40, v40
	v_lshlrev_b32_e32 v78, 16, v76
	v_and_b32_e32 v79, 0xffff0000, v76
	v_lshlrev_b32_e32 v76, 16, v77
	v_and_b32_e32 v77, 0xffff0000, v77
	v_pk_add_f32 v[76:77], v[96:97], v[76:77]
	v_pk_add_f32 v[78:79], v[94:95], v[78:79]
	v_and_b32_sdwa v96, v77, v88 dst_sel:DWORD dst_unused:UNUSED_PAD src0_sel:WORD_1 src1_sel:DWORD
	v_and_b32_sdwa v95, v78, v88 dst_sel:DWORD dst_unused:UNUSED_PAD src0_sel:WORD_1 src1_sel:DWORD
	v_and_b32_sdwa v97, v79, v88 dst_sel:DWORD dst_unused:UNUSED_PAD src0_sel:WORD_1 src1_sel:DWORD
	v_and_b32_sdwa v94, v76, v88 dst_sel:DWORD dst_unused:UNUSED_PAD src0_sel:WORD_1 src1_sel:DWORD
	v_add3_u32 v100, v78, v95, s22
	v_add3_u32 v95, v77, v96, s22
	v_add3_u32 v96, v79, v97, s22
	v_add3_u32 v94, v76, v94, s22
	v_and_b32_e32 v95, 0xffff0000, v95
	v_and_b32_e32 v96, 0xffff0000, v96
	v_or_b32_sdwa v95, v95, v94 dst_sel:DWORD dst_unused:UNUSED_PAD src0_sel:DWORD src1_sel:WORD_1
	v_or_b32_sdwa v94, v96, v100 dst_sel:DWORD dst_unused:UNUSED_PAD src0_sel:DWORD src1_sel:WORD_1
	global_store_dwordx2 v[56:57], v[94:95], off offset:3072
	v_cndmask_b32_e32 v106, v1, v155, vcc
	s_waitcnt vmcnt(7)
	v_mov_b32_e32 v74, v208
	v_mov_b32_e32 v75, v209
	v_mov_b32_e32 v94, v238
	v_mov_b32_e32 v95, v239
	v_mov_b32_e32 v96, v240
	v_mov_b32_e32 v97, v241
	s_mov_b32 s100, 0
	v_add_u32_e32 v254, s20, v2
	v_min_i32_e32 v254, 0x1fff, v254
	v_ashrrev_i32_e32 v255, 31, v254
	v_lshlrev_b64 v[250:251], 13, v[254:255]
	v_lshlrev_b64 v[252:253], 14, v[254:255]
	v_lshl_add_u64 v[250:251], v[6:7], 0, v[250:251]
	v_lshl_add_u64 v[252:253], v[4:5], 0, v[252:253]
	v_lshl_add_u64 v[242:243], v[250:251], 0, s[98:99]
	v_lshl_add_u64 v[244:245], v[252:253], 0, s[98:99]
	v_lshl_add_u64 v[246:247], v[244:245], 0, s[98:99]
	v_lshl_add_u64 v[248:249], v[246:247], 0, s[98:99]
	global_load_dwordx2 v[178:179], v[250:251], off
	global_load_dwordx2 v[180:181], v[250:251], off offset:512
	global_load_dwordx2 v[182:183], v[250:251], off offset:1024
	global_load_dwordx2 v[184:185], v[250:251], off offset:1536
	global_load_dwordx2 v[186:187], v[250:251], off offset:2048
	global_load_dwordx2 v[188:189], v[250:251], off offset:2560
	global_load_dwordx2 v[190:191], v[250:251], off offset:3072
	global_load_dwordx2 v[192:193], v[250:251], off offset:3584
	global_load_dwordx2 v[194:195], v[242:243], off
	global_load_dwordx2 v[196:197], v[242:243], off offset:512
	global_load_dwordx2 v[198:199], v[242:243], off offset:1024
	global_load_dwordx2 v[200:201], v[242:243], off offset:1536
	global_load_dwordx2 v[202:203], v[242:243], off offset:2048
	global_load_dwordx2 v[204:205], v[242:243], off offset:2560
	global_load_dwordx2 v[206:207], v[242:243], off offset:3072
	global_load_dwordx2 v[208:209], v[242:243], off offset:3584
	global_load_dwordx4 v[210:213], v[252:253], off
	global_load_dwordx4 v[214:217], v[252:253], off offset:1024
	global_load_dwordx4 v[218:221], v[252:253], off offset:2048
	global_load_dwordx4 v[222:225], v[252:253], off offset:3072
	global_load_dwordx4 v[226:229], v[244:245], off
	global_load_dwordx4 v[230:233], v[244:245], off offset:1024
	global_load_dwordx4 v[234:237], v[244:245], off offset:2048
	global_load_dwordx4 v[238:241], v[244:245], off offset:3072
	v_pk_mul_f32 v[82:83], v[30:31], v[30:31]
	s_nop 0
	v_pk_mov_b32 v[100:101], v[82:83], v[98:99] op_sel:[1,0]
	v_mov_b32_e32 v83, v99
	v_pk_add_f32 v[82:83], v[100:101], v[82:83]
	v_mul_f32_e32 v98, v35, v35
	v_mul_f32_e32 v100, v37, v37
	v_pk_fma_f32 v[98:99], v[34:35], v[34:35], v[98:99] op_sel_hi:[1,1,0]
	v_pk_fma_f32 v[100:101], v[36:37], v[36:37], v[100:101] op_sel_hi:[1,1,0]
	v_pk_add_f32 v[82:83], v[82:83], v[82:83] op_sel:[0,1] op_sel_hi:[1,0]
	v_mul_f32_e32 v99, v41, v41
	v_mul_f32_e32 v101, v38, v38
	v_mov_b32_e32 v83, v99
	v_mov_b32_e32 v99, v101
	v_mov_b32_e32 v101, v102
	v_pk_add_f32 v[82:83], v[84:85], v[82:83]
	v_pk_add_f32 v[84:85], v[98:99], v[100:101]
	v_pk_mul_f32 v[98:99], v[42:43], v[42:43]
	v_pk_add_f32 v[82:83], v[82:83], v[84:85]
	v_pk_mul_f32 v[84:85], v[44:45], v[44:45]
	v_pk_add_f32 v[82:83], v[82:83], v[82:83] op_sel:[0,1] op_sel_hi:[1,0]
	v_pk_mov_b32 v[100:101], v[98:99], v[84:85] op_sel:[1,0]
	v_mov_b32_e32 v99, v85
	v_pk_add_f32 v[84:85], v[100:101], v[98:99]
	v_mul_f32_e32 v98, v49, v49
	v_mul_f32_e32 v100, v47, v47
	v_pk_add_f32 v[84:85], v[84:85], v[84:85] op_sel:[0,1] op_sel_hi:[1,0]
	v_pk_fma_f32 v[98:99], v[48:49], v[48:49], v[98:99] op_sel_hi:[1,1,0]
	v_pk_fma_f32 v[100:101], v[46:47], v[46:47], v[100:101] op_sel_hi:[1,1,0]
	v_mul_f32_e32 v83, v54, v54
	v_mul_f32_e32 v85, v55, v55
	v_mul_f32_e32 v99, v50, v50
	v_mul_f32_e32 v101, v51, v51
	v_pk_add_f32 v[82:83], v[82:83], v[84:85]
	v_pk_add_f32 v[84:85], v[98:99], v[100:101]
	v_pk_mul_f32 v[98:99], v[60:61], v[60:61]
	v_pk_add_f32 v[82:83], v[82:83], v[84:85]
	v_pk_mul_f32 v[84:85], v[58:59], v[58:59]
	v_pk_add_f32 v[82:83], v[82:83], v[82:83] op_sel:[0,1] op_sel_hi:[1,0]
	v_pk_mov_b32 v[100:101], v[98:99], v[84:85] op_sel:[1,0]
	v_mov_b32_e32 v99, v85
	v_pk_add_f32 v[84:85], v[100:101], v[98:99]
	v_mul_f32_e32 v98, v65, v65
	v_mul_f32_e32 v100, v63, v63
	v_pk_add_f32 v[84:85], v[84:85], v[84:85] op_sel:[0,1] op_sel_hi:[1,0]
	v_pk_fma_f32 v[98:99], v[64:65], v[64:65], v[98:99] op_sel_hi:[1,1,0]
	v_pk_fma_f32 v[100:101], v[62:63], v[62:63], v[100:101] op_sel_hi:[1,1,0]
	v_mul_f32_e32 v83, v68, v68
	v_mul_f32_e32 v85, v69, v69
	v_mul_f32_e32 v99, v66, v66
	v_mul_f32_e32 v101, v67, v67
	v_pk_add_f32 v[82:83], v[82:83], v[84:85]
	v_pk_add_f32 v[84:85], v[98:99], v[100:101]
	s_nop 0
	v_pk_add_f32 v[82:83], v[82:83], v[84:85]
	v_pk_mul_f32 v[84:85], v[72:73], v[72:73]
	v_pk_add_f32 v[98:99], v[82:83], v[82:83] op_sel:[0,1] op_sel_hi:[1,0]
	v_pk_mul_f32 v[82:83], v[70:71], v[70:71]
	s_nop 0
	v_pk_mov_b32 v[100:101], v[84:85], v[82:83] op_sel:[1,0]
	v_mov_b32_e32 v85, v83
	v_pk_add_f32 v[82:83], v[100:101], v[84:85]
	v_mul_f32_e32 v84, v77, v77
	v_pk_add_f32 v[100:101], v[82:83], v[82:83] op_sel:[0,1] op_sel_hi:[1,0]
	v_mul_f32_e32 v82, v79, v79
	v_pk_fma_f32 v[104:105], v[76:77], v[76:77], v[84:85] op_sel_hi:[1,1,0]
	v_pk_fma_f32 v[102:103], v[78:79], v[78:79], v[82:83] op_sel_hi:[1,1,0]
	v_lshlrev_b32_e32 v84, 16, v74
	v_and_b32_e32 v85, 0xffff0000, v74
	v_lshlrev_b32_e32 v74, 16, v75
	v_and_b32_e32 v75, 0xffff0000, v75
	v_pk_add_f32 v[82:83], v[96:97], v[74:75]
	v_pk_add_f32 v[84:85], v[94:95], v[84:85]
	v_mul_f32_e32 v103, v82, v82
	v_mul_f32_e32 v99, v84, v84
	v_mul_f32_e32 v101, v85, v85
	v_mul_f32_e32 v105, v83, v83
	v_pk_add_f32 v[74:75], v[98:99], v[100:101]
	v_pk_add_f32 v[94:95], v[102:103], v[104:105]
	v_and_b32_sdwa v99, v83, v88 dst_sel:DWORD dst_unused:UNUSED_PAD src0_sel:WORD_1 src1_sel:DWORD
	v_pk_add_f32 v[74:75], v[74:75], v[94:95]
	v_lshlrev_b32_e32 v94, 2, v93
	v_add_f32_e32 v95, v74, v75
	ds_bpermute_b32 v96, v92, v95
	v_and_b32_sdwa v100, v85, v88 dst_sel:DWORD dst_unused:UNUSED_PAD src0_sel:WORD_1 src1_sel:DWORD
	v_and_b32_sdwa v97, v82, v88 dst_sel:DWORD dst_unused:UNUSED_PAD src0_sel:WORD_1 src1_sel:DWORD
	v_and_b32_sdwa v98, v84, v88 dst_sel:DWORD dst_unused:UNUSED_PAD src0_sel:WORD_1 src1_sel:DWORD
	v_add3_u32 v99, v83, v99, s22
	s_waitcnt lgkmcnt(0)
	v_add_f32_e32 v95, v95, v96
	ds_bpermute_b32 v96, v91, v95
	v_add3_u32 v100, v85, v100, s22
	v_add3_u32 v98, v84, v98, s22
	v_add3_u32 v97, v82, v97, s22
	v_and_b32_e32 v99, 0xffff0000, v99
	s_waitcnt lgkmcnt(0)
	v_add_f32_e32 v95, v95, v96
	ds_bpermute_b32 v96, v90, v95
	v_and_b32_e32 v100, 0xffff0000, v100
	v_or_b32_sdwa v97, v99, v97 dst_sel:DWORD dst_unused:UNUSED_PAD src0_sel:DWORD src1_sel:WORD_1
	v_lshlrev_b32_e32 v93, 2, v106
	v_lshl_add_u64 v[74:75], v[10:11], 0, v[52:53]
	s_waitcnt lgkmcnt(0)
	v_add_f32_e32 v95, v95, v96
	ds_bpermute_b32 v96, v89, v95
	v_lshl_add_u64 v[52:53], v[12:13], 0, v[80:81]
	v_add_co_u32_e32 v80, vcc, s23, v74
	s_waitcnt lgkmcnt(0)
	v_add_f32_e32 v95, v95, v96
	ds_bpermute_b32 v101, v94, v95
	v_or_b32_sdwa v96, v100, v98 dst_sel:DWORD dst_unused:UNUSED_PAD src0_sel:DWORD src1_sel:WORD_1
	global_store_dwordx2 v[56:57], v[96:97], off offset:3584
	v_addc_co_u32_e32 v81, vcc, 0, v75, vcc
	s_waitcnt lgkmcnt(0)
	v_add_f32_e32 v56, v95, v101
	ds_bpermute_b32 v57, v93, v56
	ds_read_b128 v[96:99], v86 offset:16384
	ds_read_b128 v[100:103], v86 offset:17408
	ds_read_b128 v[104:107], v86
	ds_read_b128 v[108:111], v86 offset:1024
	ds_read_b128 v[112:115], v86 offset:18432
	ds_read_b128 v[116:119], v86 offset:19456
	ds_read_b128 v[120:123], v86 offset:2048
	ds_read_b128 v[124:127], v86 offset:3072
	s_waitcnt lgkmcnt(8)
	v_add_f32_e32 v56, v56, v57
	v_fmamk_f32 v56, v56, 0x39800000, v87
	v_mul_f32_e32 v57, 0x4b800000, v56
	v_cmp_gt_f32_e32 vcc, s25, v56
	s_nop 1
	v_cndmask_b32_e32 v56, v56, v57, vcc
	v_rsq_f32_e32 v56, v56
	s_nop 0
	v_mul_f32_e32 v57, 0x45800000, v56
	v_cndmask_b32_e32 v56, v56, v57, vcc
	v_pk_mul_f32 v[16:17], v[16:17], v[56:57] op_sel_hi:[1,0]
	v_pk_mul_f32 v[14:15], v[14:15], v[56:57] op_sel_hi:[1,0]
	v_pk_mul_f32 v[20:21], v[20:21], v[56:57] op_sel_hi:[1,0]
	v_pk_mul_f32 v[18:19], v[18:19], v[56:57] op_sel_hi:[1,0]
	v_pk_mul_f32 v[24:25], v[24:25], v[56:57] op_sel_hi:[1,0]
	v_pk_mul_f32 v[22:23], v[22:23], v[56:57] op_sel_hi:[1,0]
	v_pk_mul_f32 v[28:29], v[28:29], v[56:57] op_sel_hi:[1,0]
	v_pk_mul_f32 v[26:27], v[26:27], v[56:57] op_sel_hi:[1,0]
	v_pk_mul_f32 v[166:167], v[72:73], v[56:57] op_sel_hi:[1,0]
	v_pk_mul_f32 v[170:171], v[78:79], v[56:57] op_sel_hi:[1,0]
	s_waitcnt lgkmcnt(5)
	v_pk_fma_f32 v[72:73], v[106:107], v[14:15], v[98:99]
	v_pk_fma_f32 v[78:79], v[104:105], v[16:17], v[96:97]
	v_pk_mul_f32 v[128:129], v[30:31], v[56:57] op_sel_hi:[1,0]
	v_pk_mul_f32 v[130:131], v[32:33], v[56:57] op_sel_hi:[1,0]
	v_pk_mul_f32 v[34:35], v[34:35], v[56:57] op_sel_hi:[1,0]
	v_pk_mul_f32 v[36:37], v[36:37], v[56:57] op_sel_hi:[1,0]
	v_pk_mul_f32 v[132:133], v[40:41], v[56:57] op_sel_hi:[1,0]
	v_pk_mul_f32 v[134:135], v[38:39], v[56:57] op_sel_hi:[1,0]
	v_pk_mul_f32 v[136:137], v[42:43], v[56:57] op_sel_hi:[1,0]
	v_pk_mul_f32 v[138:139], v[44:45], v[56:57] op_sel_hi:[1,0]
	v_pk_mul_f32 v[140:141], v[48:49], v[56:57] op_sel_hi:[1,0]
	v_pk_mul_f32 v[142:143], v[46:47], v[56:57] op_sel_hi:[1,0]
	v_pk_mul_f32 v[54:55], v[54:55], v[56:57] op_sel_hi:[1,0]
	v_pk_mul_f32 v[144:145], v[50:51], v[56:57] op_sel_hi:[1,0]
	v_pk_mul_f32 v[146:147], v[60:61], v[56:57] op_sel_hi:[1,0]
	v_pk_mul_f32 v[148:149], v[58:59], v[56:57] op_sel_hi:[1,0]
	v_pk_mul_f32 v[150:151], v[64:65], v[56:57] op_sel_hi:[1,0]
	v_pk_mul_f32 v[152:153], v[62:63], v[56:57] op_sel_hi:[1,0]
	v_pk_mul_f32 v[162:163], v[68:69], v[56:57] op_sel_hi:[1,0]
	v_pk_mul_f32 v[164:165], v[66:67], v[56:57] op_sel_hi:[1,0]
	v_pk_mul_f32 v[168:169], v[70:71], v[56:57] op_sel_hi:[1,0]
	v_pk_mul_f32 v[172:173], v[76:77], v[56:57] op_sel_hi:[1,0]
	v_pk_mul_f32 v[174:175], v[84:85], v[56:57] op_sel_hi:[1,0]
	v_pk_mul_f32 v[176:177], v[82:83], v[56:57] op_sel_hi:[1,0]
	s_waitcnt lgkmcnt(4)
	v_pk_fma_f32 v[56:57], v[110:111], v[18:19], v[102:103]
	v_pk_fma_f32 v[62:63], v[108:109], v[20:21], v[100:101]
	s_waitcnt lgkmcnt(1)
	v_pk_fma_f32 v[38:39], v[122:123], v[22:23], v[114:115]
	v_pk_fma_f32 v[44:45], v[120:121], v[24:25], v[112:113]
	s_waitcnt lgkmcnt(0)
	v_pk_fma_f32 v[22:23], v[126:127], v[26:27], v[118:119]
	v_pk_fma_f32 v[28:29], v[124:125], v[28:29], v[116:117]
	v_bfe_u32 v14, v78, 16, 1
	v_bfe_u32 v16, v72, 16, 1
	v_bfe_u32 v15, v79, 16, 1
	v_bfe_u32 v17, v73, 16, 1
	v_bfe_u32 v18, v62, 16, 1
	v_bfe_u32 v20, v56, 16, 1
	v_bfe_u32 v24, v44, 16, 1
	v_bfe_u32 v26, v38, 16, 1
	v_bfe_u32 v30, v28, 16, 1
	v_bfe_u32 v32, v22, 16, 1
	v_add3_u32 v14, v78, v14, s22
	v_add3_u32 v16, v72, v16, s22
	v_bfe_u32 v19, v63, 16, 1
	v_bfe_u32 v21, v57, 16, 1
	v_bfe_u32 v25, v45, 16, 1
	v_bfe_u32 v27, v39, 16, 1
	v_bfe_u32 v31, v29, 16, 1
	v_bfe_u32 v33, v23, 16, 1
	v_max_f32_e64 v40, |v78|, |v79|
	v_max_f32_e64 v41, |v72|, |v73|
	v_add3_u32 v15, v79, v15, s22
	v_add3_u32 v17, v73, v17, s22
	v_add3_u32 v18, v62, v18, s22
	v_add3_u32 v20, v56, v20, s22
	v_add3_u32 v24, v44, v24, s22
	v_add3_u32 v26, v38, v26, s22
	v_add3_u32 v30, v28, v30, s22
	v_add3_u32 v32, v22, v32, s22
	v_lshrrev_b32_e32 v14, 16, v14
	v_lshrrev_b32_e32 v16, 16, v16
	v_max_f32_e64 v42, |v62|, |v63|
	v_max_f32_e64 v43, |v56|, |v57|
	v_add3_u32 v19, v63, v19, s22
	v_add3_u32 v21, v57, v21, s22
	v_add3_u32 v25, v45, v25, s22
	v_add3_u32 v27, v39, v27, s22
	v_add3_u32 v31, v29, v31, s22
	v_add3_u32 v33, v23, v33, s22
	v_max3_f32 v40, v40, 0, v41
	v_lshrrev_b32_e32 v18, 16, v18
	v_lshrrev_b32_e32 v20, 16, v20
	v_lshrrev_b32_e32 v24, 16, v24
	v_lshrrev_b32_e32 v26, 16, v26
	v_lshrrev_b32_e32 v30, 16, v30
	v_lshrrev_b32_e32 v32, 16, v32
	v_and_or_b32 v14, v15, s21, v14
	v_and_or_b32 v15, v17, s21, v16
	v_max_f32_e64 v46, |v44|, |v45|
	v_max_f32_e64 v47, |v38|, |v39|
	v_max3_f32 v40, v40, v42, v43
	v_and_or_b32 v16, v19, s21, v18
	v_and_or_b32 v17, v21, s21, v20
	v_and_or_b32 v18, v25, s21, v24
	v_and_or_b32 v19, v27, s21, v26
	v_and_or_b32 v20, v31, s21, v30
	v_and_or_b32 v21, v33, s21, v32
	global_store_dwordx2 v[74:75], v[14:15], off
	global_store_dwordx2 v[74:75], v[16:17], off offset:512
	global_store_dwordx2 v[74:75], v[18:19], off offset:1024
	global_store_dwordx2 v[74:75], v[20:21], off offset:1536
	v_max_f32_e64 v48, |v28|, |v29|
	v_max_f32_e64 v49, |v22|, |v23|
	v_max3_f32 v24, v40, v46, v47
	v_max3_f32 v58, v24, v48, v49
	ds_read_b128 v[14:17], v86 offset:20480
	ds_read_b128 v[18:21], v86 offset:21504
	ds_read_b128 v[24:27], v86 offset:4096
	ds_read_b128 v[30:33], v86 offset:5120
	ds_read_b128 v[40:43], v86 offset:22528
	ds_read_b128 v[46:49], v86 offset:23552
	ds_read_b128 v[64:67], v86 offset:6144
	ds_read_b128 v[82:85], v86 offset:7168
	s_waitcnt lgkmcnt(5)
	v_pk_fma_f32 v[68:69], v[26:27], v[130:131], v[16:17]
	v_pk_fma_f32 v[76:77], v[24:25], v[128:129], v[14:15]
	s_waitcnt lgkmcnt(4)
	v_pk_fma_f32 v[50:51], v[32:33], v[36:37], v[20:21]
	v_pk_fma_f32 v[60:61], v[30:31], v[34:35], v[18:19]
	s_waitcnt lgkmcnt(1)
	v_pk_fma_f32 v[34:35], v[134:135], v[66:67], v[42:43]
	v_pk_fma_f32 v[42:43], v[132:133], v[64:65], v[40:41]
	s_waitcnt lgkmcnt(0)
	v_pk_fma_f32 v[18:19], v[138:139], v[84:85], v[48:49]
	v_pk_fma_f32 v[26:27], v[136:137], v[82:83], v[46:47]
	v_bfe_u32 v14, v76, 16, 1
	v_bfe_u32 v16, v68, 16, 1
	v_bfe_u32 v15, v77, 16, 1
	v_bfe_u32 v17, v69, 16, 1
	v_bfe_u32 v20, v60, 16, 1
	v_bfe_u32 v24, v50, 16, 1
	v_bfe_u32 v30, v42, 16, 1
	v_bfe_u32 v32, v34, 16, 1
	v_bfe_u32 v36, v26, 16, 1
	v_bfe_u32 v40, v18, 16, 1
	v_add3_u32 v14, v76, v14, s22
	v_add3_u32 v16, v68, v16, s22
	v_bfe_u32 v21, v61, 16, 1
	v_bfe_u32 v25, v51, 16, 1
	v_bfe_u32 v31, v43, 16, 1
	v_bfe_u32 v33, v35, 16, 1
	v_bfe_u32 v37, v27, 16, 1
	v_bfe_u32 v41, v19, 16, 1
	v_max_f32_e64 v46, |v76|, |v77|
	v_max_f32_e64 v47, |v68|, |v69|
	v_add3_u32 v15, v77, v15, s22
	v_add3_u32 v17, v69, v17, s22
	v_add3_u32 v20, v60, v20, s22
	v_add3_u32 v24, v50, v24, s22
	v_add3_u32 v30, v42, v30, s22
	v_add3_u32 v32, v34, v32, s22
	v_add3_u32 v36, v26, v36, s22
	v_add3_u32 v40, v18, v40, s22
	v_lshrrev_b32_e32 v14, 16, v14
	v_lshrrev_b32_e32 v16, 16, v16
	v_max_f32_e64 v48, |v60|, |v61|
	v_max_f32_e64 v49, |v50|, |v51|
	v_add3_u32 v21, v61, v21, s22
	v_add3_u32 v25, v51, v25, s22
	v_add3_u32 v31, v43, v31, s22
	v_add3_u32 v33, v35, v33, s22
	v_add3_u32 v37, v27, v37, s22
	v_add3_u32 v41, v19, v41, s22
	v_max3_f32 v46, v58, v46, v47
	v_lshrrev_b32_e32 v20, 16, v20
	v_lshrrev_b32_e32 v24, 16, v24
	v_lshrrev_b32_e32 v30, 16, v30
	v_lshrrev_b32_e32 v32, 16, v32
	v_lshrrev_b32_e32 v36, 16, v36
	v_lshrrev_b32_e32 v40, 16, v40
	v_and_or_b32 v14, v15, s21, v14
	v_and_or_b32 v15, v17, s21, v16
	v_max_f32_e64 v59, |v42|, |v43|
	v_max_f32_e64 v64, |v34|, |v35|
	v_max3_f32 v46, v46, v48, v49
	v_and_or_b32 v16, v21, s21, v20
	v_and_or_b32 v17, v25, s21, v24
	v_and_or_b32 v20, v31, s21, v30
	v_and_or_b32 v21, v33, s21, v32
	v_and_or_b32 v24, v37, s21, v36
	v_and_or_b32 v25, v41, s21, v40
	global_store_dwordx2 v[74:75], v[14:15], off offset:2048
	global_store_dwordx2 v[74:75], v[16:17], off offset:2560
	global_store_dwordx2 v[74:75], v[20:21], off offset:3072
	global_store_dwordx2 v[74:75], v[24:25], off offset:3584
	v_max_f32_e64 v65, |v26|, |v27|
	v_max_f32_e64 v66, |v18|, |v19|
	v_max3_f32 v30, v46, v59, v64
	v_max3_f32 v20, v30, v65, v66
	ds_read_b128 v[14:17], v86 offset:24576
	ds_read_b128 v[30:33], v86 offset:25600
	ds_read_b128 v[46:49], v86 offset:8192
	ds_read_b128 v[82:85], v86 offset:9216
	ds_read_b128 v[96:99], v86 offset:26624
	ds_read_b128 v[100:103], v86 offset:27648
	ds_read_b128 v[104:107], v86 offset:10240
	ds_read_b128 v[108:111], v86 offset:11264
	s_waitcnt lgkmcnt(5)
	v_pk_fma_f32 v[66:67], v[142:143], v[48:49], v[16:17]
	v_pk_fma_f32 v[74:75], v[140:141], v[46:47], v[14:15]
	s_waitcnt lgkmcnt(4)
	v_pk_fma_f32 v[48:49], v[144:145], v[84:85], v[32:33]
	v_pk_fma_f32 v[58:59], v[54:55], v[82:83], v[30:31]
	s_waitcnt lgkmcnt(1)
	v_pk_fma_f32 v[32:33], v[148:149], v[106:107], v[98:99]
	v_pk_fma_f32 v[40:41], v[146:147], v[104:105], v[96:97]
	s_waitcnt lgkmcnt(0)
	v_pk_fma_f32 v[16:17], v[152:153], v[110:111], v[102:103]
	v_pk_fma_f32 v[24:25], v[150:151], v[108:109], v[100:101]
	v_bfe_u32 v14, v74, 16, 1
	v_bfe_u32 v21, v66, 16, 1
	v_bfe_u32 v15, v75, 16, 1
	v_bfe_u32 v30, v67, 16, 1
	v_bfe_u32 v31, v58, 16, 1
	v_bfe_u32 v37, v48, 16, 1
	v_bfe_u32 v47, v40, 16, 1
	v_bfe_u32 v55, v32, 16, 1
	v_bfe_u32 v65, v24, 16, 1
	v_bfe_u32 v71, v16, 16, 1
	v_add3_u32 v14, v74, v14, s22
	v_add3_u32 v21, v66, v21, s22
	v_bfe_u32 v36, v59, 16, 1
	v_bfe_u32 v46, v49, 16, 1
	v_bfe_u32 v54, v41, 16, 1
	v_bfe_u32 v64, v33, 16, 1
	v_bfe_u32 v70, v25, 16, 1
	v_bfe_u32 v82, v17, 16, 1
	v_max_f32_e64 v83, |v74|, |v75|
	v_max_f32_e64 v84, |v66|, |v67|
	v_add3_u32 v15, v75, v15, s22
	v_add3_u32 v30, v67, v30, s22
	v_add3_u32 v31, v58, v31, s22
	v_add3_u32 v37, v48, v37, s22
	v_add3_u32 v47, v40, v47, s22
	v_add3_u32 v55, v32, v55, s22
	v_add3_u32 v65, v24, v65, s22
	v_add3_u32 v71, v16, v71, s22
	v_lshrrev_b32_e32 v14, 16, v14
	v_lshrrev_b32_e32 v21, 16, v21
	v_max_f32_e64 v85, |v58|, |v59|
	v_max_f32_e64 v95, |v48|, |v49|
	v_add3_u32 v36, v59, v36, s22
	v_add3_u32 v46, v49, v46, s22
	v_add3_u32 v54, v41, v54, s22
	v_add3_u32 v64, v33, v64, s22
	v_add3_u32 v70, v25, v70, s22
	v_add3_u32 v82, v17, v82, s22
	v_max3_f32 v20, v20, v83, v84
	v_lshrrev_b32_e32 v31, 16, v31
	v_lshrrev_b32_e32 v37, 16, v37
	v_lshrrev_b32_e32 v47, 16, v47
	v_lshrrev_b32_e32 v55, 16, v55
	v_lshrrev_b32_e32 v65, 16, v65
	v_lshrrev_b32_e32 v71, 16, v71
	v_and_or_b32 v14, v15, s21, v14
	v_and_or_b32 v15, v30, s21, v21
	v_max_f32_e64 v96, |v40|, |v41|
	v_max_f32_e64 v97, |v32|, |v33|
	v_max3_f32 v83, v20, v85, v95
	v_and_or_b32 v20, v36, s21, v31
	v_and_or_b32 v21, v46, s21, v37
	v_and_or_b32 v30, v54, s21, v47
	v_and_or_b32 v31, v64, s21, v55
	v_and_or_b32 v36, v70, s21, v65
	v_and_or_b32 v37, v82, s21, v71
	global_store_dwordx2 v[80:81], v[14:15], off
	global_store_dwordx2 v[80:81], v[20:21], off offset:512
	global_store_dwordx2 v[80:81], v[30:31], off offset:1024
	global_store_dwordx2 v[80:81], v[36:37], off offset:1536
	v_max_f32_e64 v98, |v24|, |v25|
	v_max_f32_e64 v99, |v16|, |v17|
	v_max3_f32 v46, v83, v96, v97
	v_max3_f32 v95, v46, v98, v99
	ds_read_b128 v[82:85], v86 offset:28672
	ds_read_b128 v[96:99], v86 offset:29696
	ds_read_b128 v[100:103], v86 offset:12288
	ds_read_b128 v[104:107], v86 offset:13312
	ds_read_b128 v[108:111], v86 offset:30720
	ds_read_b128 v[112:115], v86 offset:31744
	ds_read_b128 v[116:119], v86 offset:14336
	ds_read_b128 v[120:123], v86 offset:15360
	s_waitcnt lgkmcnt(5)
	v_pk_fma_f32 v[64:65], v[164:165], v[102:103], v[84:85]
	v_pk_fma_f32 v[70:71], v[162:163], v[100:101], v[82:83]
	s_waitcnt lgkmcnt(4)
	v_pk_fma_f32 v[46:47], v[168:169], v[106:107], v[98:99]
	v_pk_fma_f32 v[54:55], v[166:167], v[104:105], v[96:97]
	s_waitcnt lgkmcnt(1)
	v_pk_fma_f32 v[36:37], v[170:171], v[116:117], v[108:109]
	v_max_f32_e64 v108, |v70|, |v71|
	v_max_f32_e64 v109, |v64|, |v65|
	v_pk_fma_f32 v[30:31], v[172:173], v[118:119], v[110:111]
	v_max_f32_e64 v110, |v54|, |v55|
	v_max_f32_e64 v111, |v46|, |v47|
	v_max3_f32 v95, v95, v108, v109
	s_waitcnt lgkmcnt(0)
	v_pk_fma_f32 v[14:15], v[176:177], v[122:123], v[114:115]
	v_pk_fma_f32 v[20:21], v[174:175], v[120:121], v[112:113]
	v_max_f32_e64 v112, |v36|, |v37|
	v_max_f32_e64 v113, |v30|, |v31|
	v_max3_f32 v95, v95, v110, v111
	v_max_f32_e64 v114, |v20|, |v21|
	v_max_f32_e64 v115, |v14|, |v15|
	v_max3_f32 v95, v95, v112, v113
	v_max3_f32 v95, v95, v114, v115
	ds_bpermute_b32 v108, v92, v95
	v_bfe_u32 v82, v70, 16, 1
	v_bfe_u32 v84, v64, 16, 1
	v_bfe_u32 v96, v54, 16, 1
	v_bfe_u32 v83, v71, 16, 1
	s_waitcnt lgkmcnt(0)
	v_max_f32_e32 v108, v108, v108
	v_max_f32_e32 v95, v95, v108
	ds_bpermute_b32 v108, v91, v95
	v_bfe_u32 v85, v65, 16, 1
	v_bfe_u32 v97, v55, 16, 1
	v_add3_u32 v82, v70, v82, s22
	v_add3_u32 v84, v64, v84, s22
	s_waitcnt lgkmcnt(0)
	v_max_f32_e32 v108, v108, v108
	v_max_f32_e32 v95, v95, v108
	ds_bpermute_b32 v108, v90, v95
	v_add3_u32 v96, v54, v96, s22
	v_add3_u32 v83, v71, v83, s22
	v_add3_u32 v85, v65, v85, s22
	v_add3_u32 v97, v55, v97, s22
	s_waitcnt lgkmcnt(0)
	v_max_f32_e32 v108, v108, v108
	v_max_f32_e32 v95, v95, v108
	ds_bpermute_b32 v108, v89, v95
	v_lshrrev_b32_e32 v82, 16, v82
	v_lshrrev_b32_e32 v84, 16, v84
	v_lshrrev_b32_e32 v96, 16, v96
	v_and_or_b32 v82, v83, s21, v82
	v_and_or_b32 v83, v85, s21, v84
	v_and_or_b32 v84, v97, s21, v96
	s_waitcnt lgkmcnt(0)
	v_max_f32_e32 v96, v108, v108
	v_max_f32_e32 v95, v95, v96
	ds_bpermute_b32 v108, v94, v95
	v_bfe_u32 v100, v36, 16, 1
	v_bfe_u32 v101, v37, 16, 1
	v_add3_u32 v100, v36, v100, s22
	v_add3_u32 v101, v37, v101, s22
	v_lshrrev_b32_e32 v100, 16, v100
	v_and_or_b32 v96, v101, s21, v100
	s_waitcnt lgkmcnt(0)
	v_max_f32_e32 v100, v108, v108
	v_max_f32_e32 v95, v95, v100
	ds_bpermute_b32 v100, v93, v95
	v_bfe_u32 v98, v46, 16, 1
	v_bfe_u32 v102, v30, 16, 1
	v_bfe_u32 v104, v20, 16, 1
	v_bfe_u32 v106, v14, 16, 1
	v_bfe_u32 v99, v47, 16, 1
	v_bfe_u32 v103, v31, 16, 1
	v_bfe_u32 v105, v21, 16, 1
	v_bfe_u32 v107, v15, 16, 1
	v_add3_u32 v98, v46, v98, s22
	v_add3_u32 v102, v30, v102, s22
	v_add3_u32 v104, v20, v104, s22
	v_add3_u32 v106, v14, v106, s22
	v_add3_u32 v99, v47, v99, s22
	v_add3_u32 v103, v31, v103, s22
	v_add3_u32 v105, v21, v105, s22
	v_add3_u32 v107, v15, v107, s22
	v_lshrrev_b32_e32 v98, 16, v98
	v_lshrrev_b32_e32 v102, 16, v102
	v_lshrrev_b32_e32 v104, 16, v104
	v_lshrrev_b32_e32 v106, 16, v106
	v_and_or_b32 v85, v99, s21, v98
	v_and_or_b32 v97, v103, s21, v102
	v_and_or_b32 v98, v105, s21, v104
	v_and_or_b32 v99, v107, s21, v106
	global_store_dwordx2 v[80:81], v[82:83], off offset:2048
	global_store_dwordx2 v[80:81], v[84:85], off offset:2560
	global_store_dwordx2 v[80:81], v[96:97], off offset:3072
	global_store_dwordx2 v[80:81], v[98:99], off offset:3584
	s_waitcnt lgkmcnt(0)
	v_max3_f32 v80, v95, v100, s26
	v_mul_f32_e32 v80, 0x3c09ae41, v80
	v_div_scale_f32 v81, s[18:19], v80, v80, 1.0
	v_rcp_f32_e32 v82, v81
	v_div_scale_f32 v83, vcc, 1.0, v80, 1.0
	v_fma_f32 v84, -v81, v82, 1.0
	v_fmac_f32_e32 v82, v84, v82
	v_mul_f32_e32 v84, v83, v82
	v_fma_f32 v85, -v81, v84, v83
	v_fmac_f32_e32 v84, v85, v82
	v_fma_f32 v81, -v81, v84, v83
	v_div_fmas_f32 v81, v81, v82, v84
	v_div_fixup_f32 v81, v81, v80, 1.0
	v_mul_f32_e32 v78, v78, v81
	v_mul_f32_e32 v79, v79, v81
	v_mul_f32_e32 v72, v72, v81
	v_mul_f32_e32 v73, v73, v81
	v_rndne_f32_e32 v78, v78
	v_rndne_f32_e32 v79, v79
	v_mul_f32_e32 v62, v62, v81
	v_mul_f32_e32 v63, v63, v81
	v_mul_f32_e32 v57, v57, v81
	v_rndne_f32_e32 v72, v72
	v_rndne_f32_e32 v73, v73
	v_cvt_i32_f32_e32 v78, v78
	v_cvt_i32_f32_e32 v79, v79
	v_mul_f32_e32 v56, v56, v81
	v_rndne_f32_e32 v62, v62
	v_rndne_f32_e32 v63, v63
	v_rndne_f32_e32 v57, v57
	v_cvt_i32_f32_e32 v72, v72
	v_cvt_i32_f32_e32 v73, v73
	v_mul_f32_e32 v44, v44, v81
	v_mul_f32_e32 v45, v45, v81
	v_mul_f32_e32 v39, v39, v81
	v_rndne_f32_e32 v56, v56
	v_cvt_i32_f32_e32 v62, v62
	v_cvt_i32_f32_e32 v63, v63
	v_cvt_i32_f32_e32 v57, v57
	v_mul_f32_e32 v38, v38, v81
	v_rndne_f32_e32 v44, v44
	v_rndne_f32_e32 v45, v45
	v_rndne_f32_e32 v39, v39
	v_cvt_i32_f32_e32 v56, v56
	v_mul_f32_e32 v28, v28, v81
	v_mul_f32_e32 v29, v29, v81
	v_mul_f32_e32 v22, v22, v81
	v_mul_f32_e32 v23, v23, v81
	v_mul_f32_e32 v76, v76, v81
	v_mul_f32_e32 v77, v77, v81
	v_mul_f32_e32 v68, v68, v81
	v_mul_f32_e32 v69, v69, v81
	v_mul_f32_e32 v60, v60, v81
	v_mul_f32_e32 v61, v61, v81
	v_mul_f32_e32 v50, v50, v81
	v_mul_f32_e32 v51, v51, v81
	v_mul_f32_e32 v42, v42, v81
	v_mul_f32_e32 v43, v43, v81
	v_mul_f32_e32 v34, v34, v81
	v_mul_f32_e32 v35, v35, v81
	v_mul_f32_e32 v26, v26, v81
	v_mul_f32_e32 v27, v27, v81
	v_mul_f32_e32 v18, v18, v81
	v_mul_f32_e32 v19, v19, v81
	v_mul_f32_e32 v74, v74, v81
	v_mul_f32_e32 v75, v75, v81
	v_mul_f32_e32 v66, v66, v81
	v_mul_f32_e32 v67, v67, v81
	v_mul_f32_e32 v58, v58, v81
	v_mul_f32_e32 v59, v59, v81
	v_mul_f32_e32 v48, v48, v81
	v_mul_f32_e32 v49, v49, v81
	v_mul_f32_e32 v40, v40, v81
	v_mul_f32_e32 v41, v41, v81
	v_mul_f32_e32 v32, v32, v81
	v_mul_f32_e32 v33, v33, v81
	v_mul_f32_e32 v24, v24, v81
	v_mul_f32_e32 v25, v25, v81
	v_mul_f32_e32 v16, v16, v81
	v_mul_f32_e32 v17, v17, v81
	v_mul_f32_e32 v70, v70, v81
	v_mul_f32_e32 v71, v71, v81
	v_mul_f32_e32 v64, v64, v81
	v_mul_f32_e32 v65, v65, v81
	v_mul_f32_e32 v54, v54, v81
	v_mul_f32_e32 v55, v55, v81
	v_mul_f32_e32 v46, v46, v81
	v_mul_f32_e32 v47, v47, v81
	v_mul_f32_e32 v36, v36, v81
	v_mul_f32_e32 v37, v37, v81
	v_mul_f32_e32 v30, v30, v81
	v_mul_f32_e32 v31, v31, v81
	v_mul_f32_e32 v20, v20, v81
	v_mul_f32_e32 v21, v21, v81
	v_mul_f32_e32 v14, v14, v81
	v_mul_f32_e32 v15, v15, v81
	v_rndne_f32_e32 v38, v38
	v_cvt_i32_f32_e32 v44, v44
	v_cvt_i32_f32_e32 v45, v45
	v_cvt_i32_f32_e32 v39, v39
	v_add_u32_e32 v81, v79, v78
	v_rndne_f32_e32 v28, v28
	v_rndne_f32_e32 v29, v29
	v_rndne_f32_e32 v23, v23
	v_cvt_i32_f32_e32 v38, v38
	v_lshlrev_b32_e32 v82, 16, v72
	v_add3_u32 v72, v81, v73, v72
	v_rndne_f32_e32 v22, v22
	v_cvt_i32_f32_e32 v28, v28
	v_cvt_i32_f32_e32 v29, v29
	v_cvt_i32_f32_e32 v23, v23
	v_perm_b32 v85, v57, v62, s27
	v_add3_u32 v62, v72, v63, v62
	v_rndne_f32_e32 v76, v76
	v_rndne_f32_e32 v77, v77
	v_cvt_i32_f32_e32 v22, v22
	v_lshlrev_b32_e32 v84, 16, v56
	v_add3_u32 v56, v62, v57, v56
	v_rndne_f32_e32 v68, v68
	v_rndne_f32_e32 v69, v69
	v_cvt_i32_f32_e32 v76, v76
	v_cvt_i32_f32_e32 v77, v77
	v_perm_b32 v97, v39, v44, s27
	v_add3_u32 v44, v56, v45, v44
	v_rndne_f32_e32 v60, v60
	v_rndne_f32_e32 v61, v61
	v_cvt_i32_f32_e32 v68, v68
	v_cvt_i32_f32_e32 v69, v69
	v_lshlrev_b32_e32 v96, 16, v38
	v_add3_u32 v38, v44, v39, v38
	v_rndne_f32_e32 v50, v50
	v_rndne_f32_e32 v51, v51
	v_cvt_i32_f32_e32 v60, v60
	v_cvt_i32_f32_e32 v61, v61
	v_perm_b32 v100, v23, v28, s27
	v_add3_u32 v28, v38, v29, v28
	v_rndne_f32_e32 v42, v42
	v_rndne_f32_e32 v43, v43
	v_cvt_i32_f32_e32 v50, v50
	v_cvt_i32_f32_e32 v51, v51
	v_lshlrev_b32_e32 v99, 16, v22
	v_add3_u32 v22, v28, v23, v22
	v_rndne_f32_e32 v34, v34
	v_rndne_f32_e32 v35, v35
	v_cvt_i32_f32_e32 v42, v42
	v_cvt_i32_f32_e32 v43, v43
	v_add3_u32 v22, v22, v77, v76
	v_rndne_f32_e32 v26, v26
	v_rndne_f32_e32 v27, v27
	v_cvt_i32_f32_e32 v34, v34
	v_cvt_i32_f32_e32 v35, v35
	v_add3_u32 v22, v22, v69, v68
	v_rndne_f32_e32 v18, v18
	v_rndne_f32_e32 v19, v19
	v_cvt_i32_f32_e32 v26, v26
	v_cvt_i32_f32_e32 v27, v27
	v_add3_u32 v22, v22, v61, v60
	v_rndne_f32_e32 v74, v74
	v_rndne_f32_e32 v75, v75
	v_cvt_i32_f32_e32 v18, v18
	v_cvt_i32_f32_e32 v19, v19
	v_add3_u32 v22, v22, v51, v50
	v_rndne_f32_e32 v66, v66
	v_rndne_f32_e32 v67, v67
	v_cvt_i32_f32_e32 v74, v74
	v_cvt_i32_f32_e32 v75, v75
	v_add3_u32 v22, v22, v43, v42
	v_rndne_f32_e32 v58, v58
	v_rndne_f32_e32 v59, v59
	v_cvt_i32_f32_e32 v66, v66
	v_cvt_i32_f32_e32 v67, v67
	v_add3_u32 v22, v22, v35, v34
	v_rndne_f32_e32 v48, v48
	v_rndne_f32_e32 v49, v49
	v_cvt_i32_f32_e32 v58, v58
	v_cvt_i32_f32_e32 v59, v59
	v_add3_u32 v22, v22, v27, v26
	v_rndne_f32_e32 v40, v40
	v_rndne_f32_e32 v41, v41
	v_cvt_i32_f32_e32 v48, v48
	v_cvt_i32_f32_e32 v49, v49
	v_lshlrev_b32_e32 v111, 16, v18
	v_add3_u32 v18, v22, v19, v18
	v_rndne_f32_e32 v32, v32
	v_rndne_f32_e32 v33, v33
	v_cvt_i32_f32_e32 v40, v40
	v_cvt_i32_f32_e32 v41, v41
	v_add3_u32 v18, v18, v75, v74
	v_rndne_f32_e32 v24, v24
	v_rndne_f32_e32 v25, v25
	v_cvt_i32_f32_e32 v32, v32
	v_cvt_i32_f32_e32 v33, v33
	v_add3_u32 v18, v18, v67, v66
	v_rndne_f32_e32 v16, v16
	v_rndne_f32_e32 v17, v17
	v_cvt_i32_f32_e32 v24, v24
	v_cvt_i32_f32_e32 v25, v25
	v_add3_u32 v18, v18, v59, v58
	v_rndne_f32_e32 v70, v70
	v_rndne_f32_e32 v71, v71
	v_cvt_i32_f32_e32 v16, v16
	v_cvt_i32_f32_e32 v17, v17
	v_add3_u32 v18, v18, v49, v48
	v_rndne_f32_e32 v64, v64
	v_rndne_f32_e32 v65, v65
	v_cvt_i32_f32_e32 v70, v70
	v_cvt_i32_f32_e32 v71, v71
	v_add3_u32 v18, v18, v41, v40
	v_rndne_f32_e32 v54, v54
	v_rndne_f32_e32 v55, v55
	v_cvt_i32_f32_e32 v64, v64
	v_cvt_i32_f32_e32 v65, v65
	v_add3_u32 v18, v18, v33, v32
	v_rndne_f32_e32 v46, v46
	v_rndne_f32_e32 v47, v47
	v_cvt_i32_f32_e32 v54, v54
	v_cvt_i32_f32_e32 v55, v55
	v_add3_u32 v18, v18, v25, v24
	v_rndne_f32_e32 v36, v36
	v_rndne_f32_e32 v37, v37
	v_cvt_i32_f32_e32 v46, v46
	v_cvt_i32_f32_e32 v47, v47
	v_lshlrev_b32_e32 v123, 16, v16
	v_add3_u32 v16, v18, v17, v16
	v_rndne_f32_e32 v30, v30
	v_rndne_f32_e32 v31, v31
	v_cvt_i32_f32_e32 v36, v36
	v_cvt_i32_f32_e32 v37, v37
	v_add3_u32 v16, v16, v71, v70
	v_rndne_f32_e32 v20, v20
	v_rndne_f32_e32 v21, v21
	v_cvt_i32_f32_e32 v30, v30
	v_cvt_i32_f32_e32 v31, v31
	v_add3_u32 v16, v16, v65, v64
	v_rndne_f32_e32 v14, v14
	v_rndne_f32_e32 v15, v15
	v_cvt_i32_f32_e32 v20, v20
	v_cvt_i32_f32_e32 v21, v21
	v_add3_u32 v16, v16, v55, v54
	v_cvt_i32_f32_e32 v14, v14
	v_perm_b32 v124, v17, v24, s27
	v_add3_u32 v16, v16, v47, v46
	v_cvt_i32_f32_e32 v17, v15
	v_add3_u32 v15, v16, v37, v36
	v_add3_u32 v15, v15, v31, v30
	v_add3_u32 v15, v15, v21, v20
	v_add3_u32 v15, v15, v17, v14
	ds_bpermute_b32 v16, v92, v15
	v_lshlrev_b32_e32 v79, 8, v79
	v_lshlrev_b32_e32 v83, 8, v63
	v_lshlrev_b32_e32 v95, 8, v45
	v_lshlrev_b32_e32 v98, 8, v29
	s_waitcnt lgkmcnt(0)
	v_add_u32_e32 v15, v15, v16
	ds_bpermute_b32 v16, v91, v15
	v_lshlrev_b32_e32 v101, 8, v77
	v_lshlrev_b32_e32 v102, 16, v68
	v_lshlrev_b32_e32 v104, 8, v61
	v_lshlrev_b32_e32 v105, 16, v50
	s_waitcnt lgkmcnt(0)
	v_add_u32_e32 v15, v15, v16
	ds_bpermute_b32 v16, v90, v15
	v_lshlrev_b32_e32 v107, 8, v43
	v_lshlrev_b32_e32 v108, 16, v34
	v_lshlrev_b32_e32 v110, 8, v27
	v_lshlrev_b32_e32 v113, 8, v75
	s_waitcnt lgkmcnt(0)
	v_add_u32_e32 v15, v15, v16
	ds_bpermute_b32 v16, v89, v15
	v_lshlrev_b32_e32 v114, 16, v66
	v_lshlrev_b32_e32 v116, 8, v59
	v_lshlrev_b32_e32 v117, 16, v48
	v_lshlrev_b32_e32 v119, 8, v41
	v_lshlrev_b32_e32 v120, 16, v32
	v_lshlrev_b32_e32 v122, 8, v25
	v_lshlrev_b32_e32 v125, 8, v71
	v_lshlrev_b32_e32 v126, 16, v64
	v_perm_b32 v78, v73, v78, s27
	v_and_b32_e32 v73, 0xff00, v79
	v_and_b32_e32 v79, 0xff0000, v82
	v_and_b32_e32 v81, 0xff00, v83
	v_and_b32_e32 v82, 0xff0000, v84
	v_and_b32_e32 v83, 0xff00, v95
	v_and_b32_e32 v84, 0xff0000, v96
	v_and_b32_e32 v95, 0xff00, v98
	v_and_b32_e32 v96, 0xff0000, v99
	v_and_b32_e32 v98, 0xff00, v101
	v_and_b32_e32 v99, 0xff0000, v102
	v_and_b32_e32 v101, 0xff00, v104
	v_and_b32_e32 v102, 0xff0000, v105
	v_and_b32_e32 v104, 0xff00, v107
	v_and_b32_e32 v105, 0xff0000, v108
	v_and_b32_e32 v107, 0xff00, v110
	v_and_b32_e32 v108, 0xff0000, v111
	v_and_b32_e32 v110, 0xff00, v113
	v_and_b32_e32 v111, 0xff0000, v114
	v_and_b32_e32 v113, 0xff00, v116
	v_and_b32_e32 v114, 0xff0000, v117
	v_and_b32_e32 v116, 0xff00, v119
	v_and_b32_e32 v117, 0xff0000, v120
	v_and_b32_e32 v119, 0xff00, v122
	v_and_b32_e32 v120, 0xff0000, v123
	v_and_b32_e32 v122, 0xff00, v125
	v_and_b32_e32 v123, 0xff0000, v126
	v_perm_b32 v18, v65, v70, s27
	v_perm_b32 v103, v69, v76, s27
	v_perm_b32 v106, v51, v60, s27
	v_perm_b32 v109, v35, v42, s27
	v_perm_b32 v112, v19, v26, s27
	v_perm_b32 v115, v67, v74, s27
	v_perm_b32 v118, v49, v58, s27
	v_perm_b32 v121, v33, v40, s27
	v_or3_b32 v73, v78, v73, v79
	v_or3_b32 v63, v85, v81, v82
	v_or3_b32 v18, v18, v122, v123
	s_waitcnt lgkmcnt(0)
	v_add_u32_e32 v15, v15, v16
	v_or3_b32 v72, v97, v83, v84
	v_or3_b32 v78, v100, v95, v96
	v_or3_b32 v79, v103, v98, v99
	v_or3_b32 v81, v106, v101, v102
	v_or3_b32 v82, v109, v104, v105
	v_or3_b32 v83, v112, v107, v108
	v_or3_b32 v84, v115, v110, v111
	v_or3_b32 v85, v118, v113, v114
	v_or3_b32 v95, v121, v116, v117
	v_or3_b32 v96, v124, v119, v120
	global_store_dword v[52:53], v73, off
	global_store_dword v[52:53], v63, off offset:256
	global_store_dword v[52:53], v72, off offset:512
	global_store_dword v[52:53], v78, off offset:768
	global_store_dword v[52:53], v79, off offset:1024
	global_store_dword v[52:53], v81, off offset:1280
	global_store_dword v[52:53], v82, off offset:1536
	global_store_dword v[52:53], v83, off offset:1792
	global_store_dword v[52:53], v84, off offset:2048
	global_store_dword v[52:53], v85, off offset:2304
	global_store_dword v[52:53], v95, off offset:2560
	global_store_dword v[52:53], v96, off offset:2816
	global_store_dword v[52:53], v18, off offset:3072
	v_lshlrev_b32_e32 v18, 8, v55
	v_lshlrev_b32_e32 v19, 16, v46
	ds_bpermute_b32 v16, v94, v15
	v_and_b32_e32 v18, 0xff00, v18
	v_and_b32_e32 v19, 0xff0000, v19
	v_perm_b32 v22, v47, v54, s27
	v_or3_b32 v18, v22, v18, v19
	global_store_dword v[52:53], v18, off offset:3328
	v_lshlrev_b32_e32 v18, 8, v37
	v_lshlrev_b32_e32 v19, 16, v30
	v_and_b32_e32 v18, 0xff00, v18
	v_and_b32_e32 v19, 0xff0000, v19
	v_perm_b32 v22, v31, v36, s27
	v_or3_b32 v18, v22, v18, v19
	v_lshlrev_b32_e32 v19, 16, v14
	s_waitcnt lgkmcnt(0)
	v_add_u32_e32 v14, v15, v16
	ds_bpermute_b32 v15, v93, v14
	global_store_dword v[52:53], v18, off offset:3584
	v_lshlrev_b32_e32 v18, 8, v21
	v_and_b32_e32 v18, 0xff00, v18
	v_and_b32_e32 v16, 0xff0000, v19
	v_perm_b32 v17, v17, v20, s27
	v_or3_b32 v16, v17, v18, v16
	global_store_dword v[52:53], v16, off offset:3840
	s_and_saveexec_b64 s[18:19], s[8:9]
	s_cbranch_execz .LBB0_1672
	v_lshlrev_b64 v[16:17], 2, v[2:3]
	v_lshl_add_u64 v[18:19], s[12:13], 0, v[16:17]
	v_lshl_add_u64 v[16:17], s[14:15], 0, v[16:17]
	s_waitcnt lgkmcnt(0)
	v_add_u32_e32 v3, v14, v15
	global_store_dword v[18:19], v80, off
	global_store_dword v[16:17], v3, off
	s_branch .LBB0_1672
